# v14_oscale
# speedup vs baseline: 1.0278x; 1.0058x over previous
.LBB1_53:
	ds_read_b128 v[164:167], v205 offset:43008
	ds_read_b128 v[168:171], v205 offset:43040
	ds_read_b128 v[172:175], v205 offset:43072
	ds_read_b128 v[176:179], v205 offset:43104
	ds_read_b128 v[180:183], v205 offset:43136
	ds_read_b128 v[184:187], v205 offset:43168
	ds_read_b128 v[188:191], v205 offset:43200
	ds_read_b128 v[192:195], v205 offset:43232
	s_waitcnt vmcnt(17) lgkmcnt(7)
	v_mfma_f32_32x32x16_f16 v[34:49], v[112:115], v[164:167], 0
	s_waitcnt vmcnt(0)
	v_mfma_f32_32x32x16_f16 v[18:33], v[116:119], v[164:167], v[2:17]
	s_waitcnt lgkmcnt(6)
	v_mfma_f32_32x32x16_f16 v[34:49], v[100:103], v[168:171], v[34:49]
	v_mfma_f32_32x32x16_f16 v[18:33], v[120:123], v[168:171], v[18:33]
	s_waitcnt lgkmcnt(5)
	v_mfma_f32_32x32x16_f16 v[34:49], v[104:107], v[172:175], v[34:49]
	v_mfma_f32_32x32x16_f16 v[18:33], v[124:127], v[172:175], v[18:33]
	s_waitcnt lgkmcnt(4)
	v_mfma_f32_32x32x16_f16 v[34:49], v[108:111], v[176:179], v[34:49]
	v_mfma_f32_32x32x16_f16 v[18:33], v[128:131], v[176:179], v[18:33]
	s_waitcnt lgkmcnt(3)
	v_mfma_f32_32x32x16_f16 v[34:49], v[132:135], v[180:183], v[34:49]
	v_mfma_f32_32x32x16_f16 v[18:33], v[148:151], v[180:183], v[18:33]
	s_waitcnt lgkmcnt(2)
	v_mfma_f32_32x32x16_f16 v[34:49], v[136:139], v[184:187], v[34:49]
	v_mfma_f32_32x32x16_f16 v[18:33], v[152:155], v[184:187], v[18:33]
	s_waitcnt lgkmcnt(1)
	v_mfma_f32_32x32x16_f16 v[34:49], v[140:143], v[188:191], v[34:49]
	v_mfma_f32_32x32x16_f16 v[18:33], v[156:159], v[188:191], v[18:33]
	s_waitcnt lgkmcnt(0)
	v_mfma_f32_32x32x16_f16 v[34:49], v[144:147], v[192:195], v[34:49]
	v_mfma_f32_32x32x16_f16 v[18:33], v[160:163], v[192:195], v[18:33]
	s_nop 10
	v_cvt_pk_f16_f32 v41, v40, v41
	v_cvt_pk_f16_f32 v40, v38, v39
	v_cvt_pk_f16_f32 v39, v36, v37
	v_cvt_pk_f16_f32 v38, v34, v35
	v_cvt_pk_f16_f32 v25, v24, v25
	v_cvt_pk_f16_f32 v24, v22, v23
	v_cvt_pk_f16_f32 v23, v20, v21
	v_cvt_pk_f16_f32 v22, v18, v19
	v_cvt_pk_f16_f32 v21, v48, v49
	v_cvt_pk_f16_f32 v20, v46, v47
	v_cvt_pk_f16_f32 v19, v44, v45
	v_cvt_pk_f16_f32 v18, v42, v43
	v_mfma_f32_32x32x16_f16 v[50:65], v[38:41], v[22:25], 0
	v_cvt_pk_f16_f32 v25, v32, v33
	v_cvt_pk_f16_f32 v24, v30, v31
	v_cvt_pk_f16_f32 v23, v28, v29
	v_cvt_pk_f16_f32 v22, v26, v27
	s_nop 1
	v_mfma_f32_32x32x16_f16 v[34:49], v[18:21], v[22:25], 0
	v_mfma_f32_32x32x16_f16 v[18:33], v[164:167], v[96:99], 0
	v_mfma_f32_32x32x16_f16 v[18:33], v[168:171], v[76:79], v[18:33]
	s_nop 2
	v_max3_f32 v250, v50, v51, v52
	v_max3_f32 v250, v250, v53, v54
	v_max3_f32 v250, v250, v55, v56
	v_max_f32_e32 v251, v61, v61
	v_max_f32_e32 v252, v60, v60
	v_max3_f32 v250, v250, v57, v58
	v_max_f32_e32 v251, v252, v251
	v_mfma_f32_32x32x16_f16 v[18:33], v[172:175], v[72:75], v[18:33]
	v_max3_f32 v251, v250, v59, v251
	v_cndmask_b32_e64 v250, v250, v251, s[0:1]
	v_mov_b32_e32 v251, v250
	s_nop 1
	v_permlane32_swap_b32_e32 v250, v251
	v_max_f32_e32 v251, v251, v251
	v_max_f32_e32 v250, v250, v250
	v_max_f32_e32 v46, v250, v251
	v_mfma_f32_32x32x16_f16 v[18:33], v[176:179], v[68:71], v[18:33]
	v_sub_f32_e32 v47, v50, v46
	v_exp_f32_e32 v50, v47
	v_sub_f32_e32 v47, v51, v46
	v_sub_f32_e32 v48, v52, v46
	v_exp_f32_e32 v51, v47
	v_exp_f32_e32 v52, v48
	v_sub_f32_e32 v48, v53, v46
	v_sub_f32_e32 v49, v55, v46
	v_mfma_f32_32x32x16_f16 v[18:33], v[180:183], v[92:95], v[18:33]
	v_sub_f32_e32 v53, v57, v46
	v_exp_f32_e32 v55, v49
	v_sub_f32_e32 v49, v56, v46
	v_exp_f32_e32 v56, v53
	v_sub_f32_e32 v53, v58, v46
	v_exp_f32_e32 v62, v48
	v_sub_f32_e32 v48, v54, v46
	v_exp_f32_e32 v57, v53
	v_mfma_f32_32x32x16_f16 v[18:33], v[184:187], v[84:87], v[18:33]
	v_sub_f32_e32 v53, v59, v46
	v_add_f32_e32 v47, 0, v50
	v_exp_f32_e32 v48, v48
	v_exp_f32_e32 v53, v53
	v_add_f32_e32 v47, v51, v47
	v_add_f32_e32 v47, v52, v47
	v_exp_f32_e32 v49, v49
	v_add_f32_e32 v47, v62, v47
	v_mfma_f32_32x32x16_f16 v[18:33], v[188:191], v[88:91], v[18:33]
	v_add_f32_e32 v47, v48, v47
	v_cndmask_b32_e64 v58, v53, 0, s[14:15]
	v_sub_f32_e32 v53, v60, v46
	v_sub_f32_e32 v46, v61, v46
	v_add_f32_e32 v47, v55, v47
	v_exp_f32_e32 v53, v53
	v_exp_f32_e32 v46, v46
	v_add_f32_e32 v47, v49, v47
	v_mfma_f32_32x32x16_f16 v[18:33], v[192:195], v[80:83], v[18:33]
	ds_read_b128 v[192:195], v240 offset:48720
	ds_read_b128 v[188:191], v240 offset:48752
	ds_read_b128 v[184:187], v240 offset:48784
	ds_read_b128 v[180:183], v240 offset:48816
	ds_read_b128 v[176:179], v240 offset:48848
	ds_read_b128 v[172:175], v240 offset:48880
	ds_read_b128 v[168:171], v240 offset:48912
	ds_read_b128 v[164:167], v240 offset:48944
	v_add_f32_e32 v47, v56, v47
	v_add_f32_e32 v47, v57, v47
	v_add_f32_e32 v47, v58, v47
	v_cndmask_b32_e64 v59, v53, 0, s[14:15]
	v_cndmask_b32_e64 v60, v46, 0, s[14:15]
	v_cvt_pk_f16_f32 v46, v50, v51
	v_max3_f32 v50, v34, v35, v36
	v_add_f32_e32 v47, v59, v47
	v_max3_f32 v50, v50, v37, v38
	v_add_f32_e32 v53, v60, v47
	v_cvt_pk_f16_f32 v47, v52, v62
	v_max3_f32 v50, v50, v39, v40
	v_max_f32_e32 v51, v45, v45
	v_max_f32_e32 v52, v44, v44
	v_max3_f32 v50, v50, v41, v42
	v_max_f32_e32 v51, v52, v51
	v_max3_f32 v51, v50, v43, v51
	v_cndmask_b32_e64 v50, v50, v51, s[0:1]
	v_mov_b32_e32 v51, v50
	s_nop 1
	v_permlane32_swap_b32_e32 v50, v51
	s_waitcnt lgkmcnt(7)
	v_mfma_f32_32x32x16_f16 v[2:17], v[116:119], v[192:195], v[2:17]
	v_max_f32_e32 v51, v51, v51
	v_max_f32_e32 v50, v50, v50
	v_max_f32_e32 v50, v50, v51
	v_sub_f32_e32 v34, v34, v50
	v_exp_f32_e32 v52, v34
	v_sub_f32_e32 v34, v35, v50
	v_sub_f32_e32 v35, v36, v50
	s_waitcnt lgkmcnt(6)
	v_mfma_f32_32x32x16_f16 v[2:17], v[120:123], v[188:191], v[2:17]
	v_cvt_pk_f16_f32 v49, v49, v56
	v_exp_f32_e32 v56, v35
	v_sub_f32_e32 v35, v37, v50
	v_cvt_pk_f16_f32 v64, v57, v58
	v_exp_f32_e32 v57, v35
	v_sub_f32_e32 v35, v38, v50
	v_exp_f32_e32 v58, v35
	s_waitcnt lgkmcnt(5)
	v_mfma_f32_32x32x16_f16 v[2:17], v[124:127], v[184:187], v[2:17]
	v_sub_f32_e32 v35, v39, v50
	v_cvt_pk_f16_f32 v65, v59, v60
	v_exp_f32_e32 v60, v35
	v_sub_f32_e32 v35, v40, v50
	v_cvt_pk_f16_f32 v48, v48, v55
	v_exp_f32_e32 v55, v34
	v_exp_f32_e32 v62, v35
	s_waitcnt lgkmcnt(4)
	v_mfma_f32_32x32x16_f16 v[2:17], v[128:131], v[180:183], v[2:17]
	v_sub_f32_e32 v35, v41, v50
	v_exp_f32_e32 v63, v35
	v_sub_f32_e32 v35, v42, v50
	v_exp_f32_e32 v59, v35
	v_sub_f32_e32 v35, v43, v50
	v_add_f32_e32 v34, 0, v52
	v_exp_f32_e32 v35, v35
	s_waitcnt lgkmcnt(3)
	v_mfma_f32_32x32x16_f16 v[2:17], v[148:151], v[176:179], v[2:17]
	v_add_f32_e32 v34, v55, v34
	v_add_f32_e32 v34, v56, v34
	v_add_f32_e32 v34, v57, v34
	v_add_f32_e32 v34, v58, v34
	v_cndmask_b32_e64 v61, v35, 0, s[14:15]
	v_sub_f32_e32 v35, v44, v50
	v_add_f32_e32 v34, v60, v34
	s_waitcnt lgkmcnt(2)
	v_mfma_f32_32x32x16_f16 v[2:17], v[152:155], v[172:175], v[2:17]
	v_exp_f32_e32 v35, v35
	v_sub_f32_e32 v36, v45, v50
	v_cvt_pk_f16_f32 v25, v24, v25
	v_cvt_pk_f16_f32 v24, v22, v23
	v_cvt_pk_f16_f32 v23, v20, v21
	v_cvt_pk_f16_f32 v22, v18, v19
	v_add_f32_e32 v34, v62, v34
	s_waitcnt lgkmcnt(1)
	v_mfma_f32_32x32x16_f16 v[2:17], v[156:159], v[168:171], v[2:17]
	v_exp_f32_e32 v36, v36
	v_add_f32_e32 v34, v63, v34
	v_add_f32_e32 v34, v59, v34
	v_add_f32_e32 v34, v61, v34
	v_cndmask_b32_e64 v211, v35, 0, s[14:15]
	v_add_f32_e32 v18, v211, v34
	s_waitcnt lgkmcnt(0)
	v_mfma_f32_32x32x16_f16 v[2:17], v[160:163], v[164:167], v[2:17]
	v_cndmask_b32_e64 v250, v36, 0, s[14:15]
	v_cvt_pk_f16_f32 v51, v32, v33
	v_mfma_f32_32x32x16_f16 v[32:47], v[22:25], v[46:49], 0
	v_cvt_pk_f16_f32 v50, v30, v31
	v_cvt_pk_f16_f32 v49, v28, v29
	v_cvt_pk_f16_f32 v48, v26, v27
	v_mov_b32_e32 v67, v66
	v_add_f32_e32 v251, v250, v18
	v_mov_b32_e32 v54, v53
	v_mov_b32_e32 v252, v251
	v_mfma_f32_32x32x16_f16 v[32:47], v[48:51], v[64:67], v[32:47]
	v_permlane32_swap_b32_e32 v53, v54
	v_permlane32_swap_b32_e32 v251, v252
	s_and_saveexec_b64 s[2:3], s[4:5]
	s_cbranch_execz .LBB1_55
	v_add_f32_e32 v18, v53, v54
	v_rcp_f32_e32 v18, v18
	s_nop 5
	v_pk_mul_f32 v[32:33], v[32:33], v[18:19] op_sel_hi:[1,0]
	v_pk_mul_f32 v[34:35], v[34:35], v[18:19] op_sel_hi:[1,0]
	v_pk_mul_f32 v[36:37], v[36:37], v[18:19] op_sel_hi:[1,0]
	v_pk_mul_f32 v[38:39], v[38:39], v[18:19] op_sel_hi:[1,0]
	v_cvt_pk_f16_f32 v20, v32, v33
	v_cvt_pk_f16_f32 v21, v34, v35
	v_cvt_pk_f16_f32 v26, v36, v37
	v_cvt_pk_f16_f32 v27, v38, v39
	ds_write2_b64 v247, v[20:21], v[26:27] offset1:2
.LBB1_55:
	s_or_b64 exec, exec, s[2:3]
	v_cvt_pk_f16_f32 v21, v62, v63
	v_cvt_pk_f16_f32 v20, v58, v60
	v_cvt_pk_f16_f32 v19, v56, v57
	v_cvt_pk_f16_f32 v18, v52, v55
	v_cvt_pk_f16_f32 v65, v211, v250
	v_cvt_pk_f16_f32 v64, v59, v61
	v_mfma_f32_32x32x16_f16 v[18:33], v[22:25], v[18:21], 0
	v_mov_b32_e32 v67, v66
	s_nop 1
	v_mfma_f32_32x32x16_f16 v[18:33], v[48:51], v[64:67], v[18:33]
	s_and_saveexec_b64 s[2:3], s[4:5]
	s_cbranch_execz .LBB1_57
	s_nop 9
	v_add_f32_e32 v18, v251, v252
	v_rcp_f32_e32 v18, v18
	s_nop 0
	v_pk_mul_f32 v[26:27], v[26:27], v[18:19] op_sel_hi:[1,0]
	v_pk_mul_f32 v[28:29], v[28:29], v[18:19] op_sel_hi:[1,0]
	v_pk_mul_f32 v[30:31], v[30:31], v[18:19] op_sel_hi:[1,0]
	v_pk_mul_f32 v[32:33], v[32:33], v[18:19] op_sel_hi:[1,0]
	v_cvt_pk_f16_f32 v20, v26, v27
	v_cvt_pk_f16_f32 v21, v28, v29
	v_cvt_pk_f16_f32 v22, v30, v31
	v_cvt_pk_f16_f32 v23, v32, v33
	ds_write2_b64 v247, v[20:21], v[22:23] offset0:4 offset1:6
.LBB1_57:
	s_or_b64 exec, exec, s[2:3]
	s_waitcnt lgkmcnt(7)
	v_mfma_f32_32x32x16_f16 v[18:33], v[112:115], v[192:195], 0
	s_lshl_b64 s[2:3], s[36:37], 15
	v_lshl_add_u64 v[34:35], v[208:209], 0, s[2:3]
	s_waitcnt lgkmcnt(6)
	v_mfma_f32_32x32x16_f16 v[18:33], v[100:103], v[188:191], v[18:33]
	global_load_dwordx4 v[100:103], v[34:35], off
	global_load_dwordx4 v[58:61], v[34:35], off offset:1024
	global_load_dwordx4 v[54:57], v[34:35], off offset:2048
	global_load_dwordx4 v[50:53], v[34:35], off offset:3072
	s_waitcnt lgkmcnt(5)
	v_mfma_f32_32x32x16_f16 v[18:33], v[104:107], v[184:187], v[18:33]
	s_waitcnt lgkmcnt(4)
	v_mfma_f32_32x32x16_f16 v[18:33], v[108:111], v[180:183], v[18:33]
	s_waitcnt lgkmcnt(3)
	v_mfma_f32_32x32x16_f16 v[18:33], v[132:135], v[176:179], v[18:33]
	s_waitcnt lgkmcnt(2)
	v_mfma_f32_32x32x16_f16 v[18:33], v[136:139], v[172:175], v[18:33]
	s_waitcnt lgkmcnt(1)
	v_mfma_f32_32x32x16_f16 v[18:33], v[140:143], v[168:171], v[18:33]
	s_waitcnt lgkmcnt(0)
	v_mfma_f32_32x32x16_f16 v[18:33], v[144:147], v[164:167], v[18:33]
	s_nop 11
	v_cvt_pk_f16_f32 v25, v24, v25
	v_cvt_pk_f16_f32 v24, v22, v23
	v_cvt_pk_f16_f32 v23, v20, v21
	v_cvt_pk_f16_f32 v22, v18, v19
	v_cvt_pk_f16_f32 v9, v8, v9
	v_cvt_pk_f16_f32 v8, v6, v7
	v_cvt_pk_f16_f32 v7, v4, v5
	v_cvt_pk_f16_f32 v6, v2, v3
	v_cvt_pk_f16_f32 v5, v32, v33
	v_cvt_pk_f16_f32 v4, v30, v31
	v_mfma_f32_32x32x16_f16 v[34:49], v[22:25], v[6:9], 0
	v_cvt_pk_f16_f32 v3, v28, v29
	v_cvt_pk_f16_f32 v2, v26, v27
	v_cvt_pk_f16_f32 v9, v16, v17
	v_cvt_pk_f16_f32 v8, v14, v15
	v_cvt_pk_f16_f32 v7, v12, v13
	v_cvt_pk_f16_f32 v6, v10, v11
	v_mov_b32_e32 v67, v66
	s_nop 0
	v_mfma_f32_32x32x16_f16 v[18:33], v[2:5], v[6:9], 0
	s_nop 2
	v_max3_f32 v2, v34, v35, v36
	v_max3_f32 v2, v2, v37, v38
	s_nop 6
	v_max3_f32 v30, v2, v39, v40
	v_mfma_f32_32x32x16_f16 v[2:17], v[192:195], v[96:99], 0
	v_max_f32_e32 v31, v45, v45
	v_max_f32_e32 v32, v44, v44
	v_max3_f32 v30, v30, v41, v42
	v_max_f32_e32 v31, v32, v31
	v_max3_f32 v31, v30, v43, v31
	v_cndmask_b32_e64 v30, v30, v31, s[0:1]
	v_mov_b32_e32 v31, v30
	v_mfma_f32_32x32x16_f16 v[2:17], v[188:191], v[76:79], v[2:17]
	s_nop 0
	v_permlane32_swap_b32_e32 v30, v31
	v_max_f32_e32 v31, v31, v31
	v_max_f32_e32 v30, v30, v30
	v_max_f32_e32 v30, v30, v31
	v_sub_f32_e32 v31, v34, v30
	v_exp_f32_e32 v34, v31
	v_mfma_f32_32x32x16_f16 v[2:17], v[184:187], v[72:75], v[2:17]
	v_sub_f32_e32 v31, v35, v30
	v_sub_f32_e32 v33, v37, v30
	v_exp_f32_e32 v35, v31
	v_sub_f32_e32 v31, v36, v30
	v_exp_f32_e32 v36, v33
	v_sub_f32_e32 v33, v38, v30
	v_exp_f32_e32 v46, v33
	v_mfma_f32_32x32x16_f16 v[2:17], v[180:183], v[68:71], v[2:17]
	v_sub_f32_e32 v33, v39, v30
	v_sub_f32_e32 v37, v41, v30
	v_exp_f32_e32 v39, v33
	v_sub_f32_e32 v33, v40, v30
	v_exp_f32_e32 v40, v37
	v_sub_f32_e32 v37, v42, v30
	v_exp_f32_e32 v41, v37
	v_sub_f32_e32 v37, v43, v30
	v_exp_f32_e32 v37, v37
	v_mfma_f32_32x32x16_f16 v[2:17], v[176:179], v[92:95], v[2:17]
	v_exp_f32_e32 v31, v31
	v_add_f32_e32 v32, 0, v34
	v_cndmask_b32_e64 v42, v37, 0, s[14:15]
	v_sub_f32_e32 v37, v44, v30
	v_sub_f32_e32 v30, v45, v30
	v_exp_f32_e32 v30, v30
	v_add_f32_e32 v32, v35, v32
	v_mfma_f32_32x32x16_f16 v[2:17], v[172:175], v[84:87], v[2:17]
	v_add_f32_e32 v32, v31, v32
	v_cndmask_b32_e64 v44, v30, 0, s[14:15]
	v_cvt_pk_f16_f32 v30, v34, v35
	v_max3_f32 v34, v18, v19, v20
	v_max3_f32 v34, v34, v21, v22
	v_add_f32_e32 v32, v36, v32
	v_cvt_pk_f16_f32 v31, v31, v36
	v_max3_f32 v34, v34, v23, v24
	v_max_f32_e32 v35, v29, v29
	v_max_f32_e32 v36, v28, v28
	v_max3_f32 v34, v34, v25, v26
	v_max_f32_e32 v35, v36, v35
	v_max3_f32 v35, v34, v27, v35
	v_cndmask_b32_e64 v34, v34, v35, s[0:1]
	v_exp_f32_e32 v33, v33
	v_mov_b32_e32 v35, v34
	s_nop 1
	v_permlane32_swap_b32_e32 v34, v35
	v_add_f32_e32 v32, v46, v32
	v_mfma_f32_32x32x16_f16 v[2:17], v[168:171], v[88:91], v[2:17]
	v_max_f32_e32 v35, v35, v35
	v_max_f32_e32 v34, v34, v34
	v_add_f32_e32 v32, v39, v32
	v_exp_f32_e32 v37, v37
	v_max_f32_e32 v34, v34, v35
	v_add_f32_e32 v32, v33, v32
	v_sub_f32_e32 v18, v18, v34
	v_add_f32_e32 v32, v40, v32
	v_exp_f32_e32 v36, v18
	v_sub_f32_e32 v18, v19, v34
	v_sub_f32_e32 v19, v20, v34
	v_add_f32_e32 v32, v41, v32
	v_cvt_pk_f16_f32 v33, v33, v40
	v_exp_f32_e32 v40, v19
	v_sub_f32_e32 v19, v21, v34
	v_add_f32_e32 v32, v42, v32
	v_cndmask_b32_e64 v43, v37, 0, s[14:15]
	v_cvt_pk_f16_f32 v64, v41, v42
	v_exp_f32_e32 v41, v19
	v_sub_f32_e32 v19, v22, v34
	v_add_f32_e32 v32, v43, v32
	v_exp_f32_e32 v42, v19
	v_sub_f32_e32 v19, v23, v34
	v_add_f32_e32 v37, v44, v32
	v_cvt_pk_f16_f32 v65, v43, v44
	v_exp_f32_e32 v44, v19
	v_sub_f32_e32 v19, v24, v34
	v_mfma_f32_32x32x16_f16 v[2:17], v[164:167], v[80:83], v[2:17]
	v_cvt_pk_f16_f32 v32, v46, v39
	v_exp_f32_e32 v39, v18
	v_exp_f32_e32 v46, v19
	v_sub_f32_e32 v19, v25, v34
	v_exp_f32_e32 v47, v19
	v_sub_f32_e32 v19, v26, v34
	v_exp_f32_e32 v43, v19
	v_sub_f32_e32 v19, v27, v34
	v_add_f32_e32 v18, 0, v36
	v_exp_f32_e32 v19, v19
	v_add_f32_e32 v18, v39, v18
	v_add_f32_e32 v18, v40, v18
	v_add_f32_e32 v18, v41, v18
	v_add_f32_e32 v18, v42, v18
	v_cndmask_b32_e64 v45, v19, 0, s[14:15]
	v_sub_f32_e32 v19, v28, v34
	v_add_f32_e32 v18, v44, v18
	v_exp_f32_e32 v19, v19
	v_sub_f32_e32 v20, v29, v34
	v_cvt_pk_f16_f32 v9, v8, v9
	v_cvt_pk_f16_f32 v8, v6, v7
	v_cvt_pk_f16_f32 v7, v4, v5
	v_cvt_pk_f16_f32 v6, v2, v3
	v_add_f32_e32 v18, v46, v18
	v_exp_f32_e32 v20, v20
	v_add_f32_e32 v18, v47, v18
	v_add_f32_e32 v18, v43, v18
	v_add_f32_e32 v18, v45, v18
	v_cndmask_b32_e64 v48, v19, 0, s[14:15]
	v_add_f32_e32 v2, v48, v18
	v_cndmask_b32_e64 v49, v20, 0, s[14:15]
	v_cvt_pk_f16_f32 v35, v16, v17
	v_mfma_f32_32x32x16_f16 v[16:31], v[6:9], v[30:33], 0
	v_cvt_pk_f16_f32 v34, v14, v15
	v_cvt_pk_f16_f32 v33, v12, v13
	v_cvt_pk_f16_f32 v32, v10, v11
	v_add_f32_e32 v62, v49, v2
	v_mov_b32_e32 v38, v37
	v_mov_b32_e32 v63, v62
	s_nop 0
	v_permlane32_swap_b32_e32 v37, v38
	v_mfma_f32_32x32x16_f16 v[16:31], v[32:35], v[64:67], v[16:31]
	v_permlane32_swap_b32_e32 v62, v63
	s_and_saveexec_b64 s[2:3], s[4:5]
	s_cbranch_execz .LBB1_59
	v_add_f32_e32 v2, v37, v38
	v_rcp_f32_e32 v2, v2
	s_nop 6
	v_pk_mul_f32 v[16:17], v[16:17], v[2:3] op_sel_hi:[1,0]
	v_pk_mul_f32 v[18:19], v[18:19], v[2:3] op_sel_hi:[1,0]
	v_pk_mul_f32 v[20:21], v[20:21], v[2:3] op_sel_hi:[1,0]
	v_pk_mul_f32 v[22:23], v[22:23], v[2:3] op_sel_hi:[1,0]
	v_cvt_pk_f16_f32 v4, v16, v17
	v_cvt_pk_f16_f32 v5, v18, v19
	v_cvt_pk_f16_f32 v10, v20, v21
	v_cvt_pk_f16_f32 v11, v22, v23
	ds_write2_b64 v248, v[4:5], v[10:11] offset1:2
.LBB1_59:
	s_or_b64 exec, exec, s[2:3]
	v_cvt_pk_f16_f32 v5, v46, v47
	v_cvt_pk_f16_f32 v4, v42, v44
	v_cvt_pk_f16_f32 v3, v40, v41
	v_cvt_pk_f16_f32 v2, v36, v39
	v_cvt_pk_f16_f32 v65, v48, v49
	v_cvt_pk_f16_f32 v64, v43, v45
	v_mfma_f32_32x32x16_f16 v[2:17], v[6:9], v[2:5], 0
	v_mov_b32_e32 v67, v66
	s_nop 1
	v_mfma_f32_32x32x16_f16 v[2:17], v[32:35], v[64:67], v[2:17]
	s_and_saveexec_b64 s[2:3], s[4:5]
	s_cbranch_execz .LBB1_61
	s_nop 9
	v_add_f32_e32 v2, v62, v63
	v_rcp_f32_e32 v2, v2
	s_nop 0
	v_pk_mul_f32 v[10:11], v[10:11], v[2:3] op_sel_hi:[1,0]
	v_pk_mul_f32 v[12:13], v[12:13], v[2:3] op_sel_hi:[1,0]
	v_pk_mul_f32 v[14:15], v[14:15], v[2:3] op_sel_hi:[1,0]
	v_pk_mul_f32 v[16:17], v[16:17], v[2:3] op_sel_hi:[1,0]
	v_cvt_pk_f16_f32 v4, v10, v11
	v_cvt_pk_f16_f32 v5, v12, v13
	v_cvt_pk_f16_f32 v6, v14, v15
	v_cvt_pk_f16_f32 v7, v16, v17
	ds_write2_b64 v248, v[4:5], v[6:7] offset0:4 offset1:6
